# attention-A tile loop: second-half K/V staging DMAs use their own scalar bases (+1 tile); lane offsets advance once per two tiles (-2 VALU per 2 tiles)
# baseline (speedup 1.0000x reference)
.Lpro_noconv:
	s_cmp_lg_u64 s[12:13], 0
	s_cselect_b64 s[54:55], -1, 0
	s_cmp_lt_u32 s0, 2
	s_mov_b32 s0, 0x3f400000
	s_cselect_b64 s[52:53], -1, 0
	s_mov_b32 s8, s9
	v_mfma_scale_f32_32x32x64_f8f6f4 v[16:31], v[12:17], v[182:187], 0, v217, v216 op_sel_hi:[0,0,0] cbsz:2 blgp:2
	s_nop 4
	v_max_f32_e32 v52, v33, v33
	v_max_f32_e32 v53, v32, v32
	v_max_f32_e32 v52, v53, v52
	v_max3_f32 v52, v52, v34, v35
	v_max3_f32 v52, v52, v36, v37
	v_max3_f32 v52, v52, v38, v39
	v_max3_f32 v52, v52, v40, v41
	v_mfma_scale_f32_32x32x64_f8f6f4 v[16:31], v[58:63], v[176:181], v[16:31], v217, v216 op_sel_hi:[0,0,0] cbsz:2 blgp:2
	v_max3_f32 v52, v52, v42, v43
	v_max3_f32 v52, v52, v44, v45
	v_max3_f32 v52, v52, v46, v47
	s_mov_b32 s10, s9
	s_mov_b32 s11, s9
	s_mov_b32 s12, s9
	s_mov_b32 s13, s9
	s_nop 4
	v_max3_f32 v52, v52, v16, v17
	v_max3_f32 v52, v52, v18, v19
	v_max3_f32 v52, v52, v20, v21
	v_max3_f32 v52, v52, v22, v23
	v_max3_f32 v52, v52, v24, v25
	v_max3_f32 v52, v52, v26, v27
	v_max3_f32 v52, v52, v28, v29
	v_max3_f32 v52, v52, v30, v31
	v_mov_b32_e32 v53, v52
	s_nop 1
	v_permlane32_swap_b32_e32 v52, v53
	v_max_f32_e32 v53, v53, v53
	v_max_f32_e32 v52, v52, v52
	v_max_f32_e32 v52, v52, v53
	v_add_f32_e32 v53, 0x7149f2ca, v52
	v_cmp_ge_f32_e32 vcc, s0, v53
	v_max_f32_e32 v52, 0xf149f2ca, v52
	s_cmp_lg_u64 vcc, exec
	v_add_f32_e32 v52, 2.0, v52
	s_cselect_b64 vcc, -1, 0
	v_cndmask_b32_e32 v52, v219, v52, vcc
	v_add_f32_e32 v53, -4.0, v52
	s_lshl_b32 s0, s46, 2
	v_sub_f32_e32 v32, v32, v53
	v_sub_f32_e32 v33, v33, v53
	v_sub_f32_e32 v34, v34, v53
	v_sub_f32_e32 v35, v35, v53
	v_sub_f32_e32 v36, v36, v53
	v_sub_f32_e32 v37, v37, v53
	v_sub_f32_e32 v38, v38, v53
	v_sub_f32_e32 v39, v39, v53
	v_sub_f32_e32 v40, v40, v53
	v_sub_f32_e32 v41, v41, v53
	v_sub_f32_e32 v42, v42, v53
	v_sub_f32_e32 v43, v43, v53
	v_sub_f32_e32 v44, v44, v53
	v_sub_f32_e32 v45, v45, v53
	v_sub_f32_e32 v46, v46, v53
	v_sub_f32_e32 v47, v47, v53
	s_add_i32 s0, s0, 0
	s_mov_b32 s14, s9
	s_mov_b32 s15, s9
	s_mov_b32 s16, s9
	s_mov_b32 s17, s9
	s_mov_b32 s18, s9
	s_mov_b32 s19, s9
	s_mov_b32 s20, s9
	s_mov_b32 s21, s9
	s_mov_b32 s22, s9
	s_mov_b32 s23, s9
	v_mov_b64_e32 v[0:1], s[8:9]
	v_exp_f32_e32 v144, v32
	v_exp_f32_e32 v145, v33
	v_exp_f32_e32 v146, v34
	v_exp_f32_e32 v147, v35
	v_exp_f32_e32 v148, v36
	v_exp_f32_e32 v149, v37
	v_exp_f32_e32 v150, v38
	v_exp_f32_e32 v151, v39
	v_exp_f32_e32 v152, v40
	v_exp_f32_e32 v153, v41
	v_exp_f32_e32 v154, v42
	v_exp_f32_e32 v155, v43
	v_exp_f32_e32 v156, v44
	v_exp_f32_e32 v157, v45
	v_exp_f32_e32 v158, v46
	v_exp_f32_e32 v159, v47
	s_add_i32 s0, s0, 0x1c800
	v_mov_b64_e32 v[2:3], s[10:11]
	v_mov_b64_e32 v[4:5], s[12:13]
	v_mov_b64_e32 v[6:7], s[14:15]
	v_mov_b64_e32 v[8:9], s[16:17]
	v_mov_b64_e32 v[10:11], s[18:19]
	v_mov_b64_e32 v[12:13], s[20:21]
	v_mov_b64_e32 v[14:15], s[22:23]
	v_sub_f32_e32 v128, v16, v53
	s_and_b64 s[10:11], s[52:53], exec
	v_lshlrev_b32_e32 v16, 7, v48
	v_sub_f32_e32 v80, 4.0, v52
	v_sub_f32_e32 v143, v31, v53
	v_sub_f32_e32 v142, v30, v53
	v_sub_f32_e32 v141, v29, v53
	v_sub_f32_e32 v140, v28, v53
	v_sub_f32_e32 v139, v27, v53
	v_sub_f32_e32 v138, v26, v53
	v_sub_f32_e32 v137, v25, v53
	v_sub_f32_e32 v136, v24, v53
	v_sub_f32_e32 v135, v23, v53
	v_sub_f32_e32 v134, v22, v53
	v_sub_f32_e32 v133, v21, v53
	v_sub_f32_e32 v132, v20, v53
	v_sub_f32_e32 v131, v19, v53
	v_sub_f32_e32 v130, v18, v53
	v_sub_f32_e32 v129, v17, v53
	s_cselect_b32 s14, 23, 22
	v_add3_u32 v164, s85, v16, v51
	s_add_u32 s10, s78, s4
	v_add_u32_e32 v174, v49, v50
	v_mov_b64_e32 v[62:63], v[14:15]
	v_mov_b64_e32 v[46:47], v[14:15]
	v_mov_b64_e32 v[30:31], v[14:15]
	v_mov_b64_e32 v[78:79], v[14:15]
	s_mov_b32 s1, 2
	s_mov_b32 s57, 1
	s_mov_b32 s27, -2
	v_mov_b32_e32 v81, v80
	v_mov_b32_e32 v82, v80
	v_mov_b32_e32 v83, v80
	v_mov_b32_e32 v84, v80
	v_mov_b32_e32 v85, v80
	v_mov_b32_e32 v86, v80
	v_mov_b32_e32 v87, v80
	v_mov_b32_e32 v88, v80
	v_mov_b32_e32 v89, v80
	v_mov_b32_e32 v90, v80
	v_mov_b32_e32 v91, v80
	v_mov_b32_e32 v92, v80
	v_mov_b32_e32 v93, v80
	v_mov_b32_e32 v94, v80
	v_mov_b32_e32 v95, v80
	s_mov_b32 s15, 0
	v_mov_b32_e32 v165, v167
	s_addc_u32 s11, s79, s5
	v_mov_b32_e32 v175, v167
	v_mov_b64_e32 v[60:61], v[12:13]
	v_mov_b64_e32 v[58:59], v[10:11]
	v_mov_b64_e32 v[56:57], v[8:9]
	v_mov_b64_e32 v[54:55], v[6:7]
	v_mov_b64_e32 v[52:53], v[4:5]
	v_mov_b64_e32 v[50:51], v[2:3]
	v_mov_b64_e32 v[48:49], v[0:1]
	v_mov_b64_e32 v[44:45], v[12:13]
	v_mov_b64_e32 v[42:43], v[10:11]
	v_mov_b64_e32 v[40:41], v[8:9]
	v_mov_b64_e32 v[38:39], v[6:7]
	v_mov_b64_e32 v[36:37], v[4:5]
	v_mov_b64_e32 v[34:35], v[2:3]
	v_mov_b64_e32 v[32:33], v[0:1]
	v_mov_b64_e32 v[28:29], v[12:13]
	v_mov_b64_e32 v[26:27], v[10:11]
	v_mov_b64_e32 v[24:25], v[8:9]
	v_mov_b64_e32 v[22:23], v[6:7]
	v_mov_b64_e32 v[20:21], v[4:5]
	v_mov_b64_e32 v[18:19], v[2:3]
	v_mov_b64_e32 v[16:17], v[0:1]
	s_mov_b32 s16, 2
	v_mov_b64_e32 v[76:77], v[12:13]
	v_mov_b64_e32 v[74:75], v[10:11]
	v_mov_b64_e32 v[72:73], v[8:9]
	v_mov_b64_e32 v[70:71], v[6:7]
	v_mov_b64_e32 v[68:69], v[4:5]
	v_mov_b64_e32 v[66:67], v[2:3]
	v_mov_b64_e32 v[64:65], v[0:1]
	v_mbcnt_lo_u32_b32 v200, -1, 0
	v_mbcnt_hi_u32_b32 v200, -1, v200
	v_lshrrev_b32_e32 v201, 3, v200
	v_mul_lo_u32 v201, v201, s56
	v_lshlrev_b32_e32 v200, 4, v200
	v_and_b32_e32 v200, 0x70, v200
	v_lshl_or_b32 v214, v201, 2, v200
	v_mov_b32_e32 v215, v214
	s_mov_b64 s[98:99], s[58:59]
	s_add_i32 s100, s66, 0xc800
	s_lshl_b32 s101, s56, 5
	s_movk_i32 s15, 0x70
	ds_read_b128 v[228:231], v223 offset:8192
	ds_read_b64 v[232:233], v224 offset:8192
	ds_read_b128 v[234:237], v223 offset:12288
	ds_read_b64 v[238:239], v224 offset:12288
	ds_read_b128 v[240:243], v221 offset:8192
	ds_read_b64 v[244:245], v222 offset:8192
	ds_read_b128 v[246:249], v221 offset:12288
	ds_read_b64 v[250:251], v222 offset:12288
	v_mbcnt_lo_u32_b32 v200, -1, 0
	v_mbcnt_hi_u32_b32 v200, -1, v200
	v_and_b32_e32 v201, 7, v200
	v_ashrrev_i32_e32 v202, 3, v200
	v_lshlrev_b32_e32 v203, 2, v200
	v_lshl_add_u32 v204, v201, 10, s66
	v_lshlrev_b32_e32 v205, 2, v202
	v_and_b32_e32 v205, 12, v205
	v_add_u32_e32 v204, 0xc800, v204
	v_add_u32_e32 v204, v204, v205
	v_add_u32_e32 v206, v202, v203
	v_add_u32_e32 v207, 8, v206
	v_add_u32_e32 v208, 16, v206
	v_add_u32_e32 v209, 24, v206
	v_and_b32_e32 v206, 28, v206
	v_and_b32_e32 v207, 28, v207
	v_and_b32_e32 v208, 28, v208
	v_and_b32_e32 v209, 28, v209
	v_lshl_add_u32 v206, v206, 2, v204
	v_lshl_add_u32 v207, v207, 2, v204
	v_lshl_add_u32 v208, v208, 2, v204
	v_lshl_add_u32 v209, v209, 2, v204
	v_mul_u32_u24_e32 v210, s48, v202
	v_lshl_add_u32 v210, v201, 3, v210
	v_lshl_add_u32 v211, v201, 5, s0
	v_lshl_add_u32 v205, v200, 4, s89
	ds_write_b128 v205, v[206:209] offset:16384
	ds_write_b64 v205, v[210:211] offset:40960
	s_add_u32 s16, s10, 0x74802000
	s_addc_u32 s17, s11, 0
	s_add_u32 s10, s10, 0x74006000
	s_addc_u32 s11, s11, 0
	s_add_u32 s4, s10, 0x2000
	s_addc_u32 s5, s11, 0
	s_add_u32 s12, s16, 0x2000
	s_addc_u32 s13, s17, 0
	s_cmp_lg_u64 s[60:61], 0
	s_cbranch_scc1 .Lattn_top_n

.LBB0_417:
	s_add_i32 m0, s89, 0x2000
	s_barrier
	global_load_lds_dwordx4 v164, s[10:11]
	s_add_i32 m0, s89, 0x8000
	s_add_i32 s100, s100, 0x400
	global_load_lds_dwordx4 v174, s[16:17]
	s_mov_b32 m0, s100
	v_add_u32_e32 v96, -16, v215
	v_bfi_b32 v96, s15, v96, v215
	v_add_u32_e32 v215, s101, v96
	global_load_lds_dwordx4 v215, s[98:99] nt

.LBB0_428:
	s_mov_b32 m0, s89
	s_barrier
	global_load_lds_dwordx4 v164, s[4:5]
	v_add_u32_e32 v164, 0x4000, v164
	s_add_i32 m0, s89, 0x6000
	s_bfe_u32 s8, s1, 0x30000
	global_load_lds_dwordx4 v174, s[12:13]
	v_add_u32_e32 v174, 0x4000, v174
	s_cbranch_scc0 .LBB0_432
	s_add_i32 s100, s100, 0x400
	s_mov_b32 m0, s100
	v_add_u32_e32 v128, -16, v215
	v_bfi_b32 v128, s15, v128, v215
	v_add_u32_e32 v215, s101, v128
	global_load_lds_dwordx4 v215, s[98:99] nt

.LBB0_432:
	s_waitcnt vmcnt(2)
	v_mbcnt_lo_u32_b32 v138, -1, 0
	v_mbcnt_hi_u32_b32 v138, -1, v138
	s_lshr_b32 s8, s1, 3
	s_add_i32 s98, s8, -1
	s_ashr_i32 s99, s98, 31
	s_lshl_b64 s[98:99], s[98:99], s14
	v_lshl_add_u32 v138, v138, 4, s89
	s_add_u32 s98, s50, s98
	s_addc_u32 s99, s51, s99
	ds_read_b128 v[150:153], v138 offset:16384
	ds_read_b64 v[146:147], v138 offset:40960
	s_mul_hi_u32 s19, s44, s48
	s_mul_i32 s18, s44, s48
	s_add_u32 s98, s98, s18
	s_addc_u32 s99, s99, s19
	s_add_u32 s98, s98, s46
	s_addc_u32 s99, s99, s47
	s_lshl_b32 s18, s48, 3
	s_andn2_b64 vcc, exec, s[54:55]
	s_waitcnt lgkmcnt(0)
	s_cbranch_vccnz .Lfin_nog
	ds_read_b128 v[128:131], v147
	ds_read_b128 v[140:143], v147 offset:16
.Lfin_nog:
	ds_read2_b32 v[188:189], v150 offset0:0 offset1:32
	ds_read2_b32 v[190:191], v150 offset0:64 offset1:96
	ds_read2_b32 v[192:193], v150 offset0:128 offset1:160
	ds_read2_b32 v[194:195], v150 offset0:192 offset1:224
	ds_read2_b32 v[196:197], v151 offset0:0 offset1:32
	ds_read2_b32 v[198:199], v151 offset0:64 offset1:96
	ds_read2_b32 v[200:201], v151 offset0:128 offset1:160
	ds_read2_b32 v[202:203], v151 offset0:192 offset1:224
	s_waitcnt lgkmcnt(7)
	ds_read2_b32 v[204:205], v152 offset0:0 offset1:32
	ds_read2_b32 v[206:207], v152 offset0:64 offset1:96
	ds_read2_b32 v[208:209], v152 offset0:128 offset1:160
	ds_read2_b32 v[210:211], v152 offset0:192 offset1:224
	ds_read2_b32 v[154:155], v153 offset0:0 offset1:32
	ds_read2_b32 v[156:157], v153 offset0:64 offset1:96
	ds_read2_b32 v[158:159], v153 offset0:128 offset1:160
	ds_read2_b32 v[212:213], v153 offset0:192 offset1:224
	s_cbranch_vccnz .Lfin_const
	s_waitcnt lgkmcnt(0)
	v_pk_mul_f32 v[132:133], v[130:131], s[24:25] op_sel_hi:[1,0]
	v_pk_mul_f32 v[134:135], v[128:129], s[24:25] op_sel_hi:[1,0]
	v_pk_mul_f32 v[128:129], v[142:143], s[24:25] op_sel_hi:[1,0]
	v_pk_mul_f32 v[130:131], v[140:141], s[24:25] op_sel_hi:[1,0]
	v_pk_mul_f32 v[188:189], v[188:189], v[134:135]
	v_pk_mul_f32 v[190:191], v[190:191], v[132:133]
	v_pk_mul_f32 v[192:193], v[192:193], v[130:131]
	v_pk_mul_f32 v[194:195], v[194:195], v[128:129]
	v_cvt_pk_fp8_f32 v140, v188, v189
	v_cvt_pk_fp8_f32 v141, v192, v193
	v_cvt_pk_fp8_f32 v140, v190, v191 op_sel:[0,0,1]
	v_cvt_pk_fp8_f32 v141, v194, v195 op_sel:[0,0,1]
	s_nop 1
	global_store_dwordx2 v146, v[140:141], s[98:99] nt
	s_add_u32 s98, s98, s18
	s_addc_u32 s99, s99, 0
	v_pk_mul_f32 v[196:197], v[196:197], v[134:135]
	v_pk_mul_f32 v[198:199], v[198:199], v[132:133]
	v_pk_mul_f32 v[200:201], v[200:201], v[130:131]
	v_pk_mul_f32 v[202:203], v[202:203], v[128:129]
	v_cvt_pk_fp8_f32 v142, v196, v197
	v_cvt_pk_fp8_f32 v143, v200, v201
	v_cvt_pk_fp8_f32 v142, v198, v199 op_sel:[0,0,1]
	v_cvt_pk_fp8_f32 v143, v202, v203 op_sel:[0,0,1]
	s_nop 1
	global_store_dwordx2 v146, v[142:143], s[98:99] nt
	s_add_u32 s98, s98, s18
	s_addc_u32 s99, s99, 0
	v_pk_mul_f32 v[204:205], v[204:205], v[134:135]
	v_pk_mul_f32 v[206:207], v[206:207], v[132:133]
	v_pk_mul_f32 v[208:209], v[208:209], v[130:131]
	v_pk_mul_f32 v[210:211], v[210:211], v[128:129]
	v_cvt_pk_fp8_f32 v140, v204, v205
	v_cvt_pk_fp8_f32 v141, v208, v209
	v_cvt_pk_fp8_f32 v140, v206, v207 op_sel:[0,0,1]
	v_cvt_pk_fp8_f32 v141, v210, v211 op_sel:[0,0,1]
	s_nop 1
	global_store_dwordx2 v146, v[140:141], s[98:99] nt
	s_add_u32 s98, s98, s18
	s_addc_u32 s99, s99, 0
	v_pk_mul_f32 v[154:155], v[154:155], v[134:135]
	v_pk_mul_f32 v[156:157], v[156:157], v[132:133]
	v_pk_mul_f32 v[158:159], v[158:159], v[130:131]
	v_pk_mul_f32 v[212:213], v[212:213], v[128:129]
	v_cvt_pk_fp8_f32 v142, v154, v155
	v_cvt_pk_fp8_f32 v143, v158, v159
	v_cvt_pk_fp8_f32 v142, v156, v157 op_sel:[0,0,1]
	v_cvt_pk_fp8_f32 v143, v212, v213 op_sel:[0,0,1]
	s_nop 1
	global_store_dwordx2 v146, v[142:143], s[98:99] nt
	s_branch .Lfin_done
.Lfin_const:
	s_waitcnt lgkmcnt(0)
	v_pk_mul_f32 v[188:189], v[188:189], s[24:25] op_sel_hi:[1,0]
	v_pk_mul_f32 v[190:191], v[190:191], s[24:25] op_sel_hi:[1,0]
	v_pk_mul_f32 v[192:193], v[192:193], s[24:25] op_sel_hi:[1,0]
	v_pk_mul_f32 v[194:195], v[194:195], s[24:25] op_sel_hi:[1,0]
	v_cvt_pk_fp8_f32 v140, v188, v189
	v_cvt_pk_fp8_f32 v141, v192, v193
	v_cvt_pk_fp8_f32 v140, v190, v191 op_sel:[0,0,1]
	v_cvt_pk_fp8_f32 v141, v194, v195 op_sel:[0,0,1]
	s_nop 1
	global_store_dwordx2 v146, v[140:141], s[98:99] nt
	s_add_u32 s98, s98, s18
	s_addc_u32 s99, s99, 0
	v_pk_mul_f32 v[196:197], v[196:197], s[24:25] op_sel_hi:[1,0]
	v_pk_mul_f32 v[198:199], v[198:199], s[24:25] op_sel_hi:[1,0]
	v_pk_mul_f32 v[200:201], v[200:201], s[24:25] op_sel_hi:[1,0]
	v_pk_mul_f32 v[202:203], v[202:203], s[24:25] op_sel_hi:[1,0]
	v_cvt_pk_fp8_f32 v142, v196, v197
	v_cvt_pk_fp8_f32 v143, v200, v201
	v_cvt_pk_fp8_f32 v142, v198, v199 op_sel:[0,0,1]
	v_cvt_pk_fp8_f32 v143, v202, v203 op_sel:[0,0,1]
	s_nop 1
	global_store_dwordx2 v146, v[142:143], s[98:99] nt
	s_add_u32 s98, s98, s18
	s_addc_u32 s99, s99, 0
	v_pk_mul_f32 v[204:205], v[204:205], s[24:25] op_sel_hi:[1,0]
	v_pk_mul_f32 v[206:207], v[206:207], s[24:25] op_sel_hi:[1,0]
	v_pk_mul_f32 v[208:209], v[208:209], s[24:25] op_sel_hi:[1,0]
	v_pk_mul_f32 v[210:211], v[210:211], s[24:25] op_sel_hi:[1,0]
	v_cvt_pk_fp8_f32 v140, v204, v205
	v_cvt_pk_fp8_f32 v141, v208, v209
	v_cvt_pk_fp8_f32 v140, v206, v207 op_sel:[0,0,1]
	v_cvt_pk_fp8_f32 v141, v210, v211 op_sel:[0,0,1]
	s_nop 1
	global_store_dwordx2 v146, v[140:141], s[98:99] nt
	s_add_u32 s98, s98, s18
	s_addc_u32 s99, s99, 0
	v_pk_mul_f32 v[154:155], v[154:155], s[24:25] op_sel_hi:[1,0]
	v_pk_mul_f32 v[156:157], v[156:157], s[24:25] op_sel_hi:[1,0]
	v_pk_mul_f32 v[158:159], v[158:159], s[24:25] op_sel_hi:[1,0]
	v_pk_mul_f32 v[212:213], v[212:213], s[24:25] op_sel_hi:[1,0]
	v_cvt_pk_fp8_f32 v142, v154, v155
	v_cvt_pk_fp8_f32 v143, v158, v159
	v_cvt_pk_fp8_f32 v142, v156, v157 op_sel:[0,0,1]
	v_cvt_pk_fp8_f32 v143, v212, v213 op_sel:[0,0,1]
	s_nop 1
	global_store_dwordx2 v146, v[142:143], s[98:99] nt

.LBB0_420:
	v_cmp_gt_f32_e32 vcc, 1.0, v166
	s_cbranch_vccz .LBB0_424
	v_mbcnt_lo_u32_b32 v128, -1, 0
	v_mbcnt_hi_u32_b32 v128, -1, v128
	s_nop 0
	v_cmp_gt_u32_e32 vcc, 32, v128
	s_and_saveexec_b64 s[18:19], vcc
	v_lshl_add_u32 v129, v128, 2, s86
	ds_write_b32 v129, v166 offset:49152
	s_or_b64 exec, exec, s[18:19]
	v_ashrrev_i32_e32 v128, 3, v128
	v_lshlrev_b32_e32 v128, 2, v128
	v_and_b32_e32 v128, -16, v128
	s_waitcnt lgkmcnt(0)
	v_add_u32_e32 v140, s86, v128
	ds_read_b128 v[128:131], v140 offset:49248
	ds_read_b128 v[132:135], v140 offset:49216
	ds_read_b128 v[136:139], v140 offset:49184
	ds_read_b128 v[140:143], v140 offset:49152
	s_waitcnt lgkmcnt(0)
	v_pk_mul_f32 v[12:13], v[12:13], v[128:129]
	v_pk_mul_f32 v[8:9], v[8:9], v[132:133]
	v_pk_mul_f32 v[4:5], v[4:5], v[136:137]
	v_pk_mul_f32 v[14:15], v[14:15], v[130:131]
	v_pk_mul_f32 v[10:11], v[10:11], v[134:135]
	v_pk_mul_f32 v[6:7], v[6:7], v[138:139]
	v_pk_mul_f32 v[2:3], v[2:3], v[142:143]
	v_pk_mul_f32 v[0:1], v[0:1], v[140:141]
	v_pk_mul_f32 v[60:61], v[60:61], v[128:129]
	v_pk_mul_f32 v[56:57], v[56:57], v[132:133]
	v_pk_mul_f32 v[52:53], v[52:53], v[136:137]
	v_pk_mul_f32 v[62:63], v[62:63], v[130:131]
	v_pk_mul_f32 v[58:59], v[58:59], v[134:135]
	v_pk_mul_f32 v[54:55], v[54:55], v[138:139]
	v_pk_mul_f32 v[50:51], v[50:51], v[142:143]
	v_pk_mul_f32 v[48:49], v[48:49], v[140:141]
	v_pk_mul_f32 v[44:45], v[44:45], v[128:129]
	v_pk_mul_f32 v[40:41], v[40:41], v[132:133]
	v_pk_mul_f32 v[36:37], v[36:37], v[136:137]
	v_pk_mul_f32 v[46:47], v[46:47], v[130:131]
	v_pk_mul_f32 v[42:43], v[42:43], v[134:135]
	v_pk_mul_f32 v[38:39], v[38:39], v[138:139]
	v_pk_mul_f32 v[34:35], v[34:35], v[142:143]
	v_pk_mul_f32 v[32:33], v[32:33], v[140:141]
	v_pk_mul_f32 v[28:29], v[28:29], v[128:129]
	v_pk_mul_f32 v[24:25], v[24:25], v[132:133]
	v_pk_mul_f32 v[20:21], v[20:21], v[136:137]
	v_pk_mul_f32 v[30:31], v[30:31], v[130:131]
	v_pk_mul_f32 v[26:27], v[26:27], v[134:135]
	v_pk_mul_f32 v[22:23], v[22:23], v[138:139]
	v_pk_mul_f32 v[18:19], v[18:19], v[142:143]
	v_pk_mul_f32 v[16:17], v[16:17], v[140:141]
	v_pk_mul_f32 v[76:77], v[76:77], v[128:129]
	v_pk_mul_f32 v[72:73], v[72:73], v[132:133]
	v_pk_mul_f32 v[68:69], v[68:69], v[136:137]
	v_pk_mul_f32 v[78:79], v[78:79], v[130:131]
	v_pk_mul_f32 v[74:75], v[74:75], v[134:135]
	v_pk_mul_f32 v[70:71], v[70:71], v[138:139]
	v_pk_mul_f32 v[66:67], v[66:67], v[142:143]
	v_pk_mul_f32 v[64:65], v[64:65], v[140:141]
	s_branch .LBB0_424
.LBB0_438:
	v_cmp_gt_f32_e32 vcc, 1.0, v166
	s_cbranch_vccz .LBB0_442
	v_mbcnt_lo_u32_b32 v96, -1, 0
	v_mbcnt_hi_u32_b32 v96, -1, v96
	s_nop 0
	v_cmp_gt_u32_e32 vcc, 32, v96
	s_and_saveexec_b64 s[18:19], vcc
	v_lshl_add_u32 v97, v96, 2, s86
	ds_write_b32 v97, v166 offset:49152
	s_or_b64 exec, exec, s[18:19]
	v_ashrrev_i32_e32 v96, 3, v96
	v_lshlrev_b32_e32 v96, 2, v96
	v_and_b32_e32 v96, -16, v96
	s_waitcnt lgkmcnt(0)
	v_add_u32_e32 v108, s86, v96
	ds_read_b128 v[96:99], v108 offset:49248
	ds_read_b128 v[100:103], v108 offset:49216
	ds_read_b128 v[104:107], v108 offset:49184
	ds_read_b128 v[108:111], v108 offset:49152
	s_waitcnt lgkmcnt(0)
	v_pk_mul_f32 v[12:13], v[12:13], v[96:97]
	v_pk_mul_f32 v[8:9], v[8:9], v[100:101]
	v_pk_mul_f32 v[4:5], v[4:5], v[104:105]
	v_pk_mul_f32 v[14:15], v[14:15], v[98:99]
	v_pk_mul_f32 v[10:11], v[10:11], v[102:103]
	v_pk_mul_f32 v[6:7], v[6:7], v[106:107]
	v_pk_mul_f32 v[2:3], v[2:3], v[110:111]
	v_pk_mul_f32 v[0:1], v[0:1], v[108:109]
	v_pk_mul_f32 v[60:61], v[60:61], v[96:97]
	v_pk_mul_f32 v[56:57], v[56:57], v[100:101]
	v_pk_mul_f32 v[52:53], v[52:53], v[104:105]
	v_pk_mul_f32 v[62:63], v[62:63], v[98:99]
	v_pk_mul_f32 v[58:59], v[58:59], v[102:103]
	v_pk_mul_f32 v[54:55], v[54:55], v[106:107]
	v_pk_mul_f32 v[50:51], v[50:51], v[110:111]
	v_pk_mul_f32 v[48:49], v[48:49], v[108:109]
	v_pk_mul_f32 v[44:45], v[44:45], v[96:97]
	v_pk_mul_f32 v[40:41], v[40:41], v[100:101]
	v_pk_mul_f32 v[36:37], v[36:37], v[104:105]
	v_pk_mul_f32 v[46:47], v[46:47], v[98:99]
	v_pk_mul_f32 v[42:43], v[42:43], v[102:103]
	v_pk_mul_f32 v[38:39], v[38:39], v[106:107]
	v_pk_mul_f32 v[34:35], v[34:35], v[110:111]
	v_pk_mul_f32 v[32:33], v[32:33], v[108:109]
	v_pk_mul_f32 v[28:29], v[28:29], v[96:97]
	v_pk_mul_f32 v[24:25], v[24:25], v[100:101]
	v_pk_mul_f32 v[20:21], v[20:21], v[104:105]
	v_pk_mul_f32 v[30:31], v[30:31], v[98:99]
	v_pk_mul_f32 v[26:27], v[26:27], v[102:103]
	v_pk_mul_f32 v[22:23], v[22:23], v[106:107]
	v_pk_mul_f32 v[18:19], v[18:19], v[110:111]
	v_pk_mul_f32 v[16:17], v[16:17], v[108:109]
	v_pk_mul_f32 v[76:77], v[76:77], v[96:97]
	v_pk_mul_f32 v[72:73], v[72:73], v[100:101]
	v_pk_mul_f32 v[68:69], v[68:69], v[104:105]
	v_pk_mul_f32 v[78:79], v[78:79], v[98:99]
	v_pk_mul_f32 v[74:75], v[74:75], v[102:103]
	v_pk_mul_f32 v[70:71], v[70:71], v[106:107]
	v_pk_mul_f32 v[66:67], v[66:67], v[110:111]
	v_pk_mul_f32 v[64:65], v[64:65], v[108:109]
	s_branch .LBB0_442

.LBB0_417_n:
	s_add_i32 m0, s89, 0x2000
	s_barrier
	global_load_lds_dwordx4 v164, s[10:11]
	s_add_i32 m0, s89, 0x8000
	s_nop 0
	global_load_lds_dwordx4 v174, s[16:17]

.LBB0_428_n:
	s_mov_b32 m0, s89
	s_barrier
	global_load_lds_dwordx4 v164, s[4:5]
	v_add_u32_e32 v164, 0x4000, v164
	s_add_i32 m0, s89, 0x6000
	s_nop 0
	global_load_lds_dwordx4 v174, s[12:13]
	v_add_u32_e32 v174, 0x4000, v174
